# speedup vs baseline: 1.0857x; 1.0009x over previous
_Z6k_poolPKDF16_PKiS2_PKfS4_S4_Pf:
	s_load_dwordx8 s[4:11], s[0:1], 0x0
	s_load_dwordx4 s[20:23], s[0:1], 0x28
	v_mov_b32_e32 v61, 0
	s_ashr_i32 s3, s2, 31
	s_lshl_b64 s[12:13], s[2:3], 2
	v_lshrrev_b32_e32 v37, 4, v0
	v_bfe_u32 v1, v0, 3, 1
	s_waitcnt lgkmcnt(0)
	s_mov_b64 s[16:17], s[4:5]
	s_add_u32 s6, s6, s12
	s_addc_u32 s7, s7, s13
	s_lshl_b32 s12, s2, 9
	s_ashr_i32 s13, s12, 31
	s_lshl_b64 s[12:13], s[12:13], 2
	s_add_u32 s8, s8, s12
	v_add_u32_e32 v1, v1, v37
	s_addc_u32 s9, s9, s13
	v_lshlrev_b32_e32 v3, 2, v1
	global_load_dword v2, v3, s[8:9]
	global_load_dword v4, v3, s[8:9] offset:256
	global_load_dword v10, v3, s[8:9] offset:512
	global_load_dword v14, v3, s[8:9] offset:768
	global_load_dword v18, v3, s[8:9] offset:1024
	global_load_dword v24, v3, s[8:9] offset:1280
	v_min_u32_e32 v1, 63, v1
	v_lshlrev_b32_e32 v1, 2, v1
	global_load_dword v6, v3, s[8:9] offset:1536
	global_load_dword v8, v1, s[8:9] offset:1792
	v_and_b32_e32 v36, 15, v0
	v_mov_b32_e32 v13, 0
	v_lshlrev_b32_e32 v12, 4, v36
	v_lshlrev_b32_e32 v51, 4, v36
	v_lshl_add_u64 v[22:23], s[4:5], 0, v[12:13]
	v_mbcnt_lo_u32_b32 v1, -1, 0
	s_load_dwordx2 s[4:5], s[0:1], 0x20
	v_mbcnt_hi_u32_b32 v1, -1, v1
	v_and_b32_e32 v38, 63, v0
	v_and_b32_e32 v9, 56, v1
	v_lshlrev_b32_e32 v7, 2, v38
	v_cmp_eq_u32_e32 vcc, 56, v9
	s_load_dword s6, s[6:7], 0x0
	v_mov_b32_e32 v40, 0xfc00fc00
	v_cndmask_b32_e64 v9, 8, 0, vcc
	v_add_lshl_u32 v49, v9, v1, 2
	v_or_b32_e32 v41, 64, v37
	v_or_b32_e32 v46, 0x80, v37
	s_mov_b32 s3, 0xfc00
	v_or_b32_e32 v47, 0xc0, v37
	v_or_b32_e32 v48, 0x100, v37
	s_waitcnt vmcnt(7)
	v_lshl_add_u32 v3, v2, 8, v51
	s_waitcnt vmcnt(6)
	global_load_dwordx4 v[30:33], v3, s[16:17]
	v_lshl_add_u32 v3, v4, 8, v51
	s_waitcnt vmcnt(6)
	global_load_dwordx4 v[26:29], v3, s[16:17]
	v_lshl_add_u32 v3, v10, 8, v51
	s_waitcnt vmcnt(6)
	global_load_dwordx4 v[10:13], v3, s[16:17]
	v_lshl_add_u32 v3, v14, 8, v51
	s_waitcnt vmcnt(6)
	global_load_dwordx4 v[14:17], v3, s[16:17]
	v_lshl_add_u32 v3, v18, 8, v51
	s_waitcnt vmcnt(6)
	global_load_dwordx4 v[18:21], v3, s[16:17]
	v_lshl_add_u32 v3, v24, 8, v51
	global_load_dwordx4 v[2:5], v3, s[16:17]
	s_nop 0
	global_load_dword v39, v7, s[10:11]
	s_waitcnt lgkmcnt(0)
	global_load_dword v34, v7, s[4:5]
	global_load_dword v35, v7, s[4:5] offset:256
	s_waitcnt vmcnt(10)
	v_lshl_add_u32 v42, v6, 8, v51
	s_waitcnt vmcnt(9)
	v_lshl_add_u32 v44, v8, 8, v51
	global_load_dwordx4 v[22:25], v42, s[16:17]
	global_load_dwordx4 v[6:9], v44, s[16:17]
	global_load_dwordx2 v[62:63], v61, s[20:21]
	s_min_i32 s4, s6, 0x1ff
	s_waitcnt vmcnt(11)
	v_cmp_gt_i32_e32 vcc, s4, v37
	v_mov_b32_dpp v54, v30 row_shl:8 row_mask:0xf bank_mask:0xf bound_ctrl:0
	v_mov_b32_dpp v55, v31 row_shl:8 row_mask:0xf bank_mask:0xf bound_ctrl:0
	v_mov_b32_dpp v56, v32 row_shl:8 row_mask:0xf bank_mask:0xf bound_ctrl:0
	v_mov_b32_dpp v57, v33 row_shl:8 row_mask:0xf bank_mask:0xf bound_ctrl:0
	v_pk_add_f16 v30, v30, v54
	v_pk_add_f16 v31, v31, v55
	v_pk_add_f16 v32, v32, v56
	v_pk_add_f16 v33, v33, v57
	v_cndmask_b32_e32 v30, v40, v30, vcc
	v_cndmask_b32_e32 v31, v40, v31, vcc
	v_cndmask_b32_e32 v32, v40, v32, vcc
	v_cndmask_b32_e32 v33, v40, v33, vcc
	s_waitcnt vmcnt(10)
	v_cmp_gt_i32_e32 vcc, s4, v41
	v_mov_b32_dpp v54, v26 row_shl:8 row_mask:0xf bank_mask:0xf bound_ctrl:0
	v_mov_b32_dpp v55, v27 row_shl:8 row_mask:0xf bank_mask:0xf bound_ctrl:0
	v_mov_b32_dpp v56, v28 row_shl:8 row_mask:0xf bank_mask:0xf bound_ctrl:0
	v_mov_b32_dpp v57, v29 row_shl:8 row_mask:0xf bank_mask:0xf bound_ctrl:0
	v_pk_add_f16 v26, v26, v54
	v_pk_add_f16 v27, v27, v55
	v_pk_add_f16 v28, v28, v56
	v_pk_add_f16 v29, v29, v57
	v_cndmask_b32_e32 v26, v40, v26, vcc
	v_cndmask_b32_e32 v27, v40, v27, vcc
	v_cndmask_b32_e32 v28, v40, v28, vcc
	v_cndmask_b32_e32 v29, v40, v29, vcc
	v_pk_max_f16 v30, v30, v26
	v_pk_max_f16 v31, v31, v27
	v_pk_max_f16 v32, v32, v28
	v_pk_max_f16 v33, v33, v29
	s_waitcnt vmcnt(9)
	v_cmp_gt_i32_e32 vcc, s4, v46
	v_mov_b32_dpp v54, v10 row_shl:8 row_mask:0xf bank_mask:0xf bound_ctrl:0
	v_mov_b32_dpp v55, v11 row_shl:8 row_mask:0xf bank_mask:0xf bound_ctrl:0
	v_mov_b32_dpp v56, v12 row_shl:8 row_mask:0xf bank_mask:0xf bound_ctrl:0
	v_mov_b32_dpp v57, v13 row_shl:8 row_mask:0xf bank_mask:0xf bound_ctrl:0
	v_pk_add_f16 v10, v10, v54
	v_pk_add_f16 v11, v11, v55
	v_pk_add_f16 v12, v12, v56
	v_pk_add_f16 v13, v13, v57
	v_cndmask_b32_e32 v10, v40, v10, vcc
	v_cndmask_b32_e32 v11, v40, v11, vcc
	v_cndmask_b32_e32 v12, v40, v12, vcc
	v_cndmask_b32_e32 v13, v40, v13, vcc
	v_pk_max_f16 v30, v30, v10
	v_pk_max_f16 v31, v31, v11
	v_pk_max_f16 v32, v32, v12
	v_pk_max_f16 v33, v33, v13
	s_waitcnt vmcnt(8)
	v_cmp_gt_i32_e32 vcc, s4, v47
	v_mov_b32_dpp v54, v14 row_shl:8 row_mask:0xf bank_mask:0xf bound_ctrl:0
	v_mov_b32_dpp v55, v15 row_shl:8 row_mask:0xf bank_mask:0xf bound_ctrl:0
	v_mov_b32_dpp v56, v16 row_shl:8 row_mask:0xf bank_mask:0xf bound_ctrl:0
	v_mov_b32_dpp v57, v17 row_shl:8 row_mask:0xf bank_mask:0xf bound_ctrl:0
	v_pk_add_f16 v14, v14, v54
	v_pk_add_f16 v15, v15, v55
	v_pk_add_f16 v16, v16, v56
	v_pk_add_f16 v17, v17, v57
	v_cndmask_b32_e32 v14, v40, v14, vcc
	v_cndmask_b32_e32 v15, v40, v15, vcc
	v_cndmask_b32_e32 v16, v40, v16, vcc
	v_cndmask_b32_e32 v17, v40, v17, vcc
	v_pk_max_f16 v30, v30, v14
	v_pk_max_f16 v31, v31, v15
	v_pk_max_f16 v32, v32, v16
	v_pk_max_f16 v33, v33, v17
	s_waitcnt vmcnt(7)
	v_cmp_gt_i32_e32 vcc, s4, v48
	v_mov_b32_dpp v54, v18 row_shl:8 row_mask:0xf bank_mask:0xf bound_ctrl:0
	v_mov_b32_dpp v55, v19 row_shl:8 row_mask:0xf bank_mask:0xf bound_ctrl:0
	v_mov_b32_dpp v56, v20 row_shl:8 row_mask:0xf bank_mask:0xf bound_ctrl:0
	v_mov_b32_dpp v57, v21 row_shl:8 row_mask:0xf bank_mask:0xf bound_ctrl:0
	v_pk_add_f16 v18, v18, v54
	v_pk_add_f16 v19, v19, v55
	v_pk_add_f16 v20, v20, v56
	v_pk_add_f16 v21, v21, v57
	v_cndmask_b32_e32 v18, v40, v18, vcc
	v_cndmask_b32_e32 v19, v40, v19, vcc
	v_cndmask_b32_e32 v20, v40, v20, vcc
	v_cndmask_b32_e32 v21, v40, v21, vcc
	v_pk_max_f16 v30, v30, v18
	v_pk_max_f16 v31, v31, v19
	v_pk_max_f16 v32, v32, v20
	v_pk_max_f16 v33, v33, v21
	v_or_b32_e32 v52, 0x140, v37
	s_waitcnt vmcnt(6)
	v_cmp_gt_i32_e32 vcc, s4, v52
	v_mov_b32_dpp v54, v2 row_shl:8 row_mask:0xf bank_mask:0xf bound_ctrl:0
	v_mov_b32_dpp v55, v3 row_shl:8 row_mask:0xf bank_mask:0xf bound_ctrl:0
	v_mov_b32_dpp v56, v4 row_shl:8 row_mask:0xf bank_mask:0xf bound_ctrl:0
	v_mov_b32_dpp v57, v5 row_shl:8 row_mask:0xf bank_mask:0xf bound_ctrl:0
	v_pk_add_f16 v2, v2, v54
	v_pk_add_f16 v3, v3, v55
	v_pk_add_f16 v4, v4, v56
	v_pk_add_f16 v5, v5, v57
	v_cndmask_b32_e32 v2, v40, v2, vcc
	v_cndmask_b32_e32 v3, v40, v3, vcc
	v_cndmask_b32_e32 v4, v40, v4, vcc
	v_cndmask_b32_e32 v5, v40, v5, vcc
	v_pk_max_f16 v30, v30, v2
	v_pk_max_f16 v31, v31, v3
	v_pk_max_f16 v32, v32, v4
	v_pk_max_f16 v33, v33, v5
	v_or_b32_e32 v52, 0x180, v37
	s_waitcnt vmcnt(2)
	v_cmp_gt_i32_e32 vcc, s4, v52
	v_mov_b32_dpp v54, v22 row_shl:8 row_mask:0xf bank_mask:0xf bound_ctrl:0
	v_mov_b32_dpp v55, v23 row_shl:8 row_mask:0xf bank_mask:0xf bound_ctrl:0
	v_mov_b32_dpp v56, v24 row_shl:8 row_mask:0xf bank_mask:0xf bound_ctrl:0
	v_mov_b32_dpp v57, v25 row_shl:8 row_mask:0xf bank_mask:0xf bound_ctrl:0
	v_pk_add_f16 v22, v22, v54
	v_pk_add_f16 v23, v23, v55
	v_pk_add_f16 v24, v24, v56
	v_pk_add_f16 v25, v25, v57
	v_cndmask_b32_e32 v22, v40, v22, vcc
	v_cndmask_b32_e32 v23, v40, v23, vcc
	v_cndmask_b32_e32 v24, v40, v24, vcc
	v_cndmask_b32_e32 v25, v40, v25, vcc
	v_pk_max_f16 v30, v30, v22
	v_pk_max_f16 v31, v31, v23
	v_pk_max_f16 v32, v32, v24
	v_pk_max_f16 v33, v33, v25
	v_or_b32_e32 v52, 0x1c0, v37
	s_waitcnt vmcnt(1)
	v_cmp_gt_i32_e32 vcc, s4, v52
	v_mov_b32_dpp v54, v6 row_shl:8 row_mask:0xf bank_mask:0xf bound_ctrl:0
	v_mov_b32_dpp v55, v7 row_shl:8 row_mask:0xf bank_mask:0xf bound_ctrl:0
	v_mov_b32_dpp v56, v8 row_shl:8 row_mask:0xf bank_mask:0xf bound_ctrl:0
	v_mov_b32_dpp v57, v9 row_shl:8 row_mask:0xf bank_mask:0xf bound_ctrl:0
	v_pk_add_f16 v6, v6, v54
	v_pk_add_f16 v7, v7, v55
	v_pk_add_f16 v8, v8, v56
	v_pk_add_f16 v9, v9, v57
	v_cndmask_b32_e32 v6, v40, v6, vcc
	v_cndmask_b32_e32 v7, v40, v7, vcc
	v_cndmask_b32_e32 v8, v40, v8, vcc
	v_cndmask_b32_e32 v9, v40, v9, vcc
	v_pk_max_f16 v30, v30, v6
	v_pk_max_f16 v31, v31, v7
	v_pk_max_f16 v32, v32, v8
	v_pk_max_f16 v33, v33, v9
	v_mov_b32_e32 v2, v30
	v_mov_b32_e32 v6, v31
	v_mov_b32_e32 v7, v32
	v_mov_b32_e32 v9, v33
	v_and_b32_e32 v4, 64, v1
	v_xor_b32_e32 v3, 16, v1
	v_add_u32_e32 v4, 64, v4
	v_cmp_lt_i32_e32 vcc, v3, v4
	s_nop 1
	v_cndmask_b32_e32 v3, v1, v3, vcc
	v_lshlrev_b32_e32 v8, 2, v3
	ds_bpermute_b32 v5, v8, v2
	v_xor_b32_e32 v3, 32, v1
	ds_bpermute_b32 v11, v8, v6
	v_cmp_lt_i32_e32 vcc, v3, v4
	s_nop 1
	v_cndmask_b32_e32 v3, v1, v3, vcc
	v_lshlrev_b32_e32 v10, 2, v3
	s_waitcnt lgkmcnt(1)
	v_pk_max_f16 v3, v5, v5
	s_waitcnt lgkmcnt(0)
	v_pk_max_f16 v5, v11, v11
	v_pk_max_f16 v3, v2, v3
	ds_bpermute_b32 v2, v8, v7
	ds_bpermute_b32 v11, v8, v9
	v_pk_max_f16 v5, v6, v5
	ds_bpermute_b32 v4, v10, v3
	ds_bpermute_b32 v6, v10, v5
	s_waitcnt lgkmcnt(3)
	v_pk_max_f16 v2, v2, v2
	v_cmp_gt_u32_e32 vcc, 8, v38
	v_pk_max_f16 v7, v7, v2
	s_waitcnt lgkmcnt(2)
	v_pk_max_f16 v2, v11, v11
	ds_bpermute_b32 v8, v10, v7
	v_pk_max_f16 v9, v9, v2
	ds_bpermute_b32 v10, v10, v9
	v_lshlrev_b32_e32 v2, 2, v0
	s_and_saveexec_b64 s[4:5], vcc
	s_cbranch_execz .LBB2_2
	s_waitcnt lgkmcnt(0)
	v_pk_max_f16 v10, v10, v10
	v_pk_max_f16 v9, v9, v9
	v_pk_max_f16 v8, v8, v8
	v_pk_max_f16 v7, v7, v7
	v_pk_max_f16 v6, v6, v6
	v_pk_max_f16 v5, v5, v5
	v_pk_max_f16 v4, v4, v4
	v_pk_max_f16 v3, v3, v3
	v_pk_max_f16 v11, v9, v10
	v_pk_max_f16 v9, v7, v8
	v_pk_max_f16 v7, v5, v6
	v_pk_max_f16 v3, v3, v4
	v_cvt_f32_f16_e32 v6, v7
	v_cvt_f32_f16_e32 v4, v3
	v_cvt_f32_f16_sdwa v5, v3 dst_sel:DWORD dst_unused:UNUSED_PAD src0_sel:WORD_1
	v_cvt_f32_f16_sdwa v7, v7 dst_sel:DWORD dst_unused:UNUSED_PAD src0_sel:WORD_1
	v_cvt_f32_f16_e32 v8, v9
	v_cvt_f32_f16_sdwa v9, v9 dst_sel:DWORD dst_unused:UNUSED_PAD src0_sel:WORD_1
	v_cvt_f32_f16_e32 v10, v11
	v_cvt_f32_f16_sdwa v11, v11 dst_sel:DWORD dst_unused:UNUSED_PAD src0_sel:WORD_1
	v_and_b32_e32 v3, 0xf00, v2
	v_lshl_add_u32 v3, v36, 5, v3
	ds_write_b128 v3, v[4:7]
	ds_write_b128 v3, v[8:11] offset:16
